# baseline (speedup 1.0000x reference)
.Lmask_ready:
	s_sub_u32 s26, 0x1ff, s2
	s_mul_i32 s26, s26, 7
	s_lshr_b32 s26, s26, 6
	s_min_u32 s26, s26, 64
	s_cmp_lt_u32 s2, 64
	s_cselect_b32 s26, 0, s26
	s_cmp_eq_u32 s26, 0
	s_cbranch_scc1 .Lhold_done
